# dilated attention: waves 4-7 item-loop start stagger s_sleep 64 instead of 32
# speedup vs baseline: 1.0266x; 1.0051x over previous
.LBB0_286:
	s_or_b64 exec, exec, s[4:5]
	s_ashr_i32 s5, s7, 9
	s_and_b32 s24, s5, -2
	s_ashr_i32 s75, s7, 6
	s_lshr_b32 s5, 16, s24
	s_and_b32 s74, s6, 3
	s_ashr_i32 s4, s3, 3
	s_and_b32 s3, s75, 15
	s_sub_i32 s6, 4, s24
	s_add_i32 s5, s5, -1
	s_lshr_b32 s25, s3, s6
	s_and_b32 s3, s5, s3
	s_ashr_i32 s5, s4, 31
	s_lshl_b64 s[20:21], s[4:5], 12
	s_lshr_b32 s6, 0x400, s24
	s_or_b32 s4, s20, s25
	s_mul_i32 s6, s6, s74
	s_lshl_b32 s3, s3, 6
	s_mul_hi_u32 s26, s4, 0x1800
	s_mul_i32 s76, s21, 0x1800
	s_add_i32 s3, s3, s6
	s_lshl_b64 s[22:23], 8, s24
	s_mul_i32 s25, s4, 0x1800
	s_add_i32 s26, s26, s76
	s_add_u32 s25, s10, s25
	s_addc_u32 s26, s11, s26
	s_lshl_b32 s27, s16, 6
	s_lshl_b32 s16, s16, 7
	s_add_u32 s25, s25, s16
	v_sub_co_u32_e64 v2, s[6:7], s3, 64
	s_addc_u32 s26, s26, 0
	s_and_b64 s[6:7], s[6:7], exec
	v_readfirstlane_b32 s6, v2
	s_cselect_b32 s6, s3, s6
	s_ashr_i32 s7, s6, 31
	s_lshl_b64 s[6:7], s[6:7], s24
	v_bfe_u32 v3, v0, 3, 3
	s_mulk_i32 s7, 0x1800
	s_mul_hi_u32 s28, s6, 0x1800
	v_lshlrev_b32_e32 v3, s24, v3
	s_add_i32 s28, s28, s7
	s_mulk_i32 s6, 0x1800
	v_mul_lo_u32 v3, v3, s49
	v_lshlrev_b32_e32 v180, 3, v0
	s_add_u32 s6, s25, s6
	v_and_or_b32 v168, v180, 56, v3
	s_addc_u32 s7, s26, s28
	v_lshl_add_u64 v[2:3], v[168:169], 1, s[6:7]
	v_lshl_add_u64 v[4:5], v[2:3], 0, s[18:19]
	v_mad_u64_u32 v[6:7], s[6:7], s22, v172, v[4:5]
	s_mul_i32 s6, s23, 0x1800
	s_nop 0
	v_add_u32_e32 v7, s6, v7
	v_mad_u64_u32 v[8:9], s[6:7], s22, v173, v[4:5]
	s_mul_i32 s6, s23, 0x3000
	s_waitcnt lgkmcnt(0)
	s_barrier
	v_add_u32_e32 v9, s6, v9
	global_load_dwordx4 v[128:131], v[6:7], off
	global_load_dwordx4 v[132:135], v[8:9], off
	v_mad_u64_u32 v[6:7], s[6:7], s22, v174, v[4:5]
	s_mul_i32 s6, s23, 0x4800
	s_nop 0
	v_add_u32_e32 v7, s6, v7
	v_mad_u64_u32 v[8:9], s[6:7], s22, v175, v[4:5]
	s_mul_i32 s6, s23, 0x6000
	s_nop 0
	v_add_u32_e32 v9, s6, v9
	global_load_dwordx4 v[136:139], v[6:7], off
	global_load_dwordx4 v[140:143], v[8:9], off
	v_mad_u64_u32 v[6:7], s[6:7], s22, v176, v[4:5]
	s_mul_i32 s6, s23, 0x7800
	v_and_b32_e32 v1, 31, v0
	v_add_u32_e32 v7, s6, v7
	v_mad_u64_u32 v[8:9], s[6:7], s22, v177, v[4:5]
	s_mul_i32 s6, s23, 0x9000
	v_add_u32_e32 v168, s3, v1
	s_mov_b32 s5, s21
	v_add_u32_e32 v9, s6, v9
	global_load_dwordx4 v[144:147], v[6:7], off
	global_load_dwordx4 v[152:155], v[8:9], off
	v_mad_u64_u32 v[4:5], s[6:7], s22, v178, v[4:5]
	v_lshlrev_b64 v[6:7], s24, v[168:169]
	s_mul_i32 s6, s23, 0xa800
	v_lshl_add_u64 v[6:7], v[6:7], 0, s[4:5]
	v_add_u32_e32 v5, s6, v5
	v_mad_u64_u32 v[8:9], s[6:7], v6, s56, v[170:171]
	v_mov_b32_e32 v6, v9
	v_mad_u64_u32 v[6:7], s[6:7], v7, s56, v[6:7]
	v_add_co_u32_e32 v2, vcc, s57, v2
	v_mov_b32_e32 v9, v6
	v_lshrrev_b32_e32 v1, 1, v0
	v_addc_co_u32_e32 v3, vcc, 0, v3, vcc
	v_lshl_add_u64 v[6:7], v[8:9], 0, s[16:17]
	v_and_b32_e32 v8, 16, v1
	v_mov_b32_e32 v9, v169
	v_add_u32_e32 v168, 32, v168
	v_lshl_add_u64 v[6:7], v[6:7], 0, v[8:9]
	global_load_dwordx4 v[148:151], v[2:3], off
	global_load_dwordx4 v[96:99], v[6:7], off offset:3072
	global_load_dwordx4 v[100:103], v[6:7], off offset:3104
	global_load_dwordx4 v[104:107], v[6:7], off offset:3136
	v_lshlrev_b64 v[2:3], s24, v[168:169]
	v_lshl_add_u64 v[2:3], v[2:3], 0, s[4:5]
	v_mad_u64_u32 v[10:11], s[4:5], v2, s56, v[170:171]
	v_mov_b32_e32 v2, v11
	v_mad_u64_u32 v[2:3], s[4:5], v3, s56, v[2:3]
	v_mov_b32_e32 v11, v2
	v_lshl_add_u64 v[2:3], v[10:11], 0, s[16:17]
	v_lshl_add_u64 v[2:3], v[2:3], 0, v[8:9]
	global_load_dwordx4 v[108:111], v[6:7], off offset:3168
	global_load_dwordx4 v[112:115], v[2:3], off offset:3072
	global_load_dwordx4 v[116:119], v[2:3], off offset:3104
	global_load_dwordx4 v[120:123], v[2:3], off offset:3136
	global_load_dwordx4 v[156:159], v[4:5], off
	global_load_dwordx4 v[124:127], v[2:3], off offset:3168
	s_lshl_b32 s3, s75, 8
	s_lshl_b32 s4, s75, 13
	s_add_i32 s79, s4, 0
	s_add_i32 s81, s3, 0
	s_add_i32 s80, s79, 0x10000
	s_add_i32 s81, s81, 0x21000
	s_add_u32 s22, s10, s16
	v_and_b32_e32 v181, 63, v0
	s_mov_b32 s78, 0
	s_addc_u32 s23, s11, 0
	s_lshl_b32 s77, s27, 1
	s_cmp_lt_u32 s75, 4
	s_cbranch_scc1 .Ldil_nostag
	s_sleep 64
